# EpiGate2 mid(): gate loads batched 5 chunks deep with counted vmcnt waits, on top of v040
# speedup vs baseline: 1.0007x; 1.0007x over previous
.LBB0_1124:
	v_readlane_b32 s74, v255, 18
	s_andn2_b64 vcc, exec, s[20:21]
	v_readlane_b32 s75, v255, 19
	s_mov_b64 s[76:77], 0x2000
	s_cbranch_vccnz .LBB0_1126
	v_mov_b64_e32 v[158:159], s[12:13]
	v_mad_i64_i32 v[154:155], s[20:21], v132, s30, v[158:159]
	v_lshlrev_b64 v[152:153], 1, v[134:135]
	v_lshl_add_u64 v[176:177], v[154:155], 0, v[152:153]
	v_mov_b64_e32 v[154:155], s[14:15]
	v_mad_i64_i32 v[132:133], s[20:21], v132, s30, v[154:155]
	v_lshl_add_u64 v[166:167], v[132:133], 0, v[152:153]
	v_mov_b32_e32 v180, s30
	v_mov_b32_e32 v181, 0
	v_mul_u32_u24_e32 v178, 0x50, v180
	v_mov_b32_e32 v179, 0
	v_lshlrev_b32_e32 v180, 4, v180
	global_load_dwordx4 v[132:135], v[176:177], off
	global_load_dwordx4 v[136:139], v[166:167], off
	global_load_dwordx4 v[150:153], v[176:177], off offset:256
	global_load_dwordx4 v[154:157], v[166:167], off offset:256
	v_lshl_add_u64 v[176:177], v[176:177], 0, v[180:181]
	v_lshl_add_u64 v[166:167], v[166:167], 0, v[180:181]
	global_load_dwordx4 v[158:161], v[176:177], off
	global_load_dwordx4 v[162:165], v[166:167], off
	global_load_dwordx4 v[172:175], v[176:177], off offset:256
	global_load_dwordx4 v[230:233], v[166:167], off offset:256
	v_lshl_add_u64 v[176:177], v[176:177], 0, v[180:181]
	v_lshl_add_u64 v[166:167], v[166:167], 0, v[180:181]
	global_load_dwordx4 v[234:237], v[176:177], off
	global_load_dwordx4 v[238:241], v[166:167], off
	s_waitcnt vmcnt(8)
	v_lshlrev_b32_e32 v246, 16, v136
	v_and_b32_e32 v247, 0xffff0000, v136
	v_lshlrev_b32_e32 v250, 16, v137
	v_and_b32_e32 v251, 0xffff0000, v137
	v_max_f32_e32 v246, 0xda24260, v246
	v_max_f32_e32 v247, 0xda24260, v247
	v_max_f32_e32 v250, 0xda24260, v250
	v_max_f32_e32 v251, 0xda24260, v251
	v_rcp_f32_e32 v246, v246
	v_rcp_f32_e32 v247, v247
	v_rcp_f32_e32 v250, v250
	v_rcp_f32_e32 v251, v251
	v_lshlrev_b32_e32 v248, 16, v132
	v_and_b32_e32 v249, 0xffff0000, v132
	v_lshlrev_b32_e32 v252, 16, v133
	v_and_b32_e32 v253, 0xffff0000, v133
	v_pk_mul_f32 v[246:247], v[246:247], v[248:249]
	v_pk_mul_f32 v[250:251], v[250:251], v[252:253]
	v_pk_mul_f32 v[128:129], v[128:129], v[246:247]
	v_pk_mul_f32 v[130:131], v[130:131], v[250:251]
	v_lshlrev_b32_e32 v246, 16, v138
	v_and_b32_e32 v247, 0xffff0000, v138
	v_lshlrev_b32_e32 v250, 16, v139
	v_and_b32_e32 v251, 0xffff0000, v139
	v_max_f32_e32 v246, 0xda24260, v246
	v_max_f32_e32 v247, 0xda24260, v247
	v_max_f32_e32 v250, 0xda24260, v250
	v_max_f32_e32 v251, 0xda24260, v251
	v_rcp_f32_e32 v246, v246
	v_rcp_f32_e32 v247, v247
	v_rcp_f32_e32 v250, v250
	v_rcp_f32_e32 v251, v251
	v_lshlrev_b32_e32 v248, 16, v134
	v_and_b32_e32 v249, 0xffff0000, v134
	v_lshlrev_b32_e32 v252, 16, v135
	v_and_b32_e32 v253, 0xffff0000, v135
	v_pk_mul_f32 v[246:247], v[246:247], v[248:249]
	v_pk_mul_f32 v[250:251], v[250:251], v[252:253]
	v_pk_mul_f32 v[124:125], v[124:125], v[246:247]
	v_pk_mul_f32 v[126:127], v[126:127], v[250:251]
	global_load_dwordx4 v[132:135], v[176:177], off offset:256
	global_load_dwordx4 v[136:139], v[166:167], off offset:256
	v_lshl_add_u64 v[176:177], v[176:177], 0, v[180:181]
	v_lshl_add_u64 v[166:167], v[166:167], 0, v[180:181]
	s_waitcnt vmcnt(8)
	v_lshlrev_b32_e32 v246, 16, v154
	v_and_b32_e32 v247, 0xffff0000, v154
	v_lshlrev_b32_e32 v250, 16, v155
	v_and_b32_e32 v251, 0xffff0000, v155
	v_max_f32_e32 v246, 0xda24260, v246
	v_max_f32_e32 v247, 0xda24260, v247
	v_max_f32_e32 v250, 0xda24260, v250
	v_max_f32_e32 v251, 0xda24260, v251
	v_rcp_f32_e32 v246, v246
	v_rcp_f32_e32 v247, v247
	v_rcp_f32_e32 v250, v250
	v_rcp_f32_e32 v251, v251
	v_lshlrev_b32_e32 v248, 16, v150
	v_and_b32_e32 v249, 0xffff0000, v150
	v_lshlrev_b32_e32 v252, 16, v151
	v_and_b32_e32 v253, 0xffff0000, v151
	v_pk_mul_f32 v[246:247], v[246:247], v[248:249]
	v_pk_mul_f32 v[250:251], v[250:251], v[252:253]
	v_pk_mul_f32 v[96:97], v[96:97], v[246:247]
	v_pk_mul_f32 v[98:99], v[98:99], v[250:251]
	v_lshlrev_b32_e32 v246, 16, v156
	v_and_b32_e32 v247, 0xffff0000, v156
	v_lshlrev_b32_e32 v250, 16, v157
	v_and_b32_e32 v251, 0xffff0000, v157
	v_max_f32_e32 v246, 0xda24260, v246
	v_max_f32_e32 v247, 0xda24260, v247
	v_max_f32_e32 v250, 0xda24260, v250
	v_max_f32_e32 v251, 0xda24260, v251
	v_rcp_f32_e32 v246, v246
	v_rcp_f32_e32 v247, v247
	v_rcp_f32_e32 v250, v250
	v_rcp_f32_e32 v251, v251
	v_lshlrev_b32_e32 v248, 16, v152
	v_and_b32_e32 v249, 0xffff0000, v152
	v_lshlrev_b32_e32 v252, 16, v153
	v_and_b32_e32 v253, 0xffff0000, v153
	v_pk_mul_f32 v[246:247], v[246:247], v[248:249]
	v_pk_mul_f32 v[250:251], v[250:251], v[252:253]
	v_pk_mul_f32 v[92:93], v[92:93], v[246:247]
	v_pk_mul_f32 v[94:95], v[94:95], v[250:251]
	global_load_dwordx4 v[150:153], v[176:177], off
	global_load_dwordx4 v[154:157], v[166:167], off
	s_waitcnt vmcnt(8)
	v_lshlrev_b32_e32 v246, 16, v162
	v_and_b32_e32 v247, 0xffff0000, v162
	v_lshlrev_b32_e32 v250, 16, v163
	v_and_b32_e32 v251, 0xffff0000, v163
	v_max_f32_e32 v246, 0xda24260, v246
	v_max_f32_e32 v247, 0xda24260, v247
	v_max_f32_e32 v250, 0xda24260, v250
	v_max_f32_e32 v251, 0xda24260, v251
	v_rcp_f32_e32 v246, v246
	v_rcp_f32_e32 v247, v247
	v_rcp_f32_e32 v250, v250
	v_rcp_f32_e32 v251, v251
	v_lshlrev_b32_e32 v248, 16, v158
	v_and_b32_e32 v249, 0xffff0000, v158
	v_lshlrev_b32_e32 v252, 16, v159
	v_and_b32_e32 v253, 0xffff0000, v159
	v_pk_mul_f32 v[246:247], v[246:247], v[248:249]
	v_pk_mul_f32 v[250:251], v[250:251], v[252:253]
	v_pk_mul_f32 v[120:121], v[120:121], v[246:247]
	v_pk_mul_f32 v[122:123], v[122:123], v[250:251]
	v_lshlrev_b32_e32 v246, 16, v164
	v_and_b32_e32 v247, 0xffff0000, v164
	v_lshlrev_b32_e32 v250, 16, v165
	v_and_b32_e32 v251, 0xffff0000, v165
	v_max_f32_e32 v246, 0xda24260, v246
	v_max_f32_e32 v247, 0xda24260, v247
	v_max_f32_e32 v250, 0xda24260, v250
	v_max_f32_e32 v251, 0xda24260, v251
	v_rcp_f32_e32 v246, v246
	v_rcp_f32_e32 v247, v247
	v_rcp_f32_e32 v250, v250
	v_rcp_f32_e32 v251, v251
	v_lshlrev_b32_e32 v248, 16, v160
	v_and_b32_e32 v249, 0xffff0000, v160
	v_lshlrev_b32_e32 v252, 16, v161
	v_and_b32_e32 v253, 0xffff0000, v161
	v_pk_mul_f32 v[246:247], v[246:247], v[248:249]
	v_pk_mul_f32 v[250:251], v[250:251], v[252:253]
	v_pk_mul_f32 v[116:117], v[116:117], v[246:247]
	v_pk_mul_f32 v[118:119], v[118:119], v[250:251]
	global_load_dwordx4 v[158:161], v[176:177], off offset:256
	global_load_dwordx4 v[162:165], v[166:167], off offset:256
	v_lshl_add_u64 v[176:177], v[176:177], 0, v[178:179]
	v_lshl_add_u64 v[166:167], v[166:167], 0, v[178:179]
	s_waitcnt vmcnt(8)
	v_lshlrev_b32_e32 v246, 16, v230
	v_and_b32_e32 v247, 0xffff0000, v230
	v_lshlrev_b32_e32 v250, 16, v231
	v_and_b32_e32 v251, 0xffff0000, v231
	v_max_f32_e32 v246, 0xda24260, v246
	v_max_f32_e32 v247, 0xda24260, v247
	v_max_f32_e32 v250, 0xda24260, v250
	v_max_f32_e32 v251, 0xda24260, v251
	v_rcp_f32_e32 v246, v246
	v_rcp_f32_e32 v247, v247
	v_rcp_f32_e32 v250, v250
	v_rcp_f32_e32 v251, v251
	v_lshlrev_b32_e32 v248, 16, v172
	v_and_b32_e32 v249, 0xffff0000, v172
	v_lshlrev_b32_e32 v252, 16, v173
	v_and_b32_e32 v253, 0xffff0000, v173
	v_pk_mul_f32 v[246:247], v[246:247], v[248:249]
	v_pk_mul_f32 v[250:251], v[250:251], v[252:253]
	v_pk_mul_f32 v[88:89], v[88:89], v[246:247]
	v_pk_mul_f32 v[90:91], v[90:91], v[250:251]
	v_lshlrev_b32_e32 v246, 16, v232
	v_and_b32_e32 v247, 0xffff0000, v232
	v_lshlrev_b32_e32 v250, 16, v233
	v_and_b32_e32 v251, 0xffff0000, v233
	v_max_f32_e32 v246, 0xda24260, v246
	v_max_f32_e32 v247, 0xda24260, v247
	v_max_f32_e32 v250, 0xda24260, v250
	v_max_f32_e32 v251, 0xda24260, v251
	v_rcp_f32_e32 v246, v246
	v_rcp_f32_e32 v247, v247
	v_rcp_f32_e32 v250, v250
	v_rcp_f32_e32 v251, v251
	v_lshlrev_b32_e32 v248, 16, v174
	v_and_b32_e32 v249, 0xffff0000, v174
	v_lshlrev_b32_e32 v252, 16, v175
	v_and_b32_e32 v253, 0xffff0000, v175
	v_pk_mul_f32 v[246:247], v[246:247], v[248:249]
	v_pk_mul_f32 v[250:251], v[250:251], v[252:253]
	v_pk_mul_f32 v[84:85], v[84:85], v[246:247]
	v_pk_mul_f32 v[86:87], v[86:87], v[250:251]
	global_load_dwordx4 v[172:175], v[176:177], off
	global_load_dwordx4 v[230:233], v[166:167], off
	s_waitcnt vmcnt(8)
	v_lshlrev_b32_e32 v246, 16, v238
	v_and_b32_e32 v247, 0xffff0000, v238
	v_lshlrev_b32_e32 v250, 16, v239
	v_and_b32_e32 v251, 0xffff0000, v239
	v_max_f32_e32 v246, 0xda24260, v246
	v_max_f32_e32 v247, 0xda24260, v247
	v_max_f32_e32 v250, 0xda24260, v250
	v_max_f32_e32 v251, 0xda24260, v251
	v_rcp_f32_e32 v246, v246
	v_rcp_f32_e32 v247, v247
	v_rcp_f32_e32 v250, v250
	v_rcp_f32_e32 v251, v251
	v_lshlrev_b32_e32 v248, 16, v234
	v_and_b32_e32 v249, 0xffff0000, v234
	v_lshlrev_b32_e32 v252, 16, v235
	v_and_b32_e32 v253, 0xffff0000, v235
	v_pk_mul_f32 v[246:247], v[246:247], v[248:249]
	v_pk_mul_f32 v[250:251], v[250:251], v[252:253]
	v_pk_mul_f32 v[112:113], v[112:113], v[246:247]
	v_pk_mul_f32 v[114:115], v[114:115], v[250:251]
	v_lshlrev_b32_e32 v246, 16, v240
	v_and_b32_e32 v247, 0xffff0000, v240
	v_lshlrev_b32_e32 v250, 16, v241
	v_and_b32_e32 v251, 0xffff0000, v241
	v_max_f32_e32 v246, 0xda24260, v246
	v_max_f32_e32 v247, 0xda24260, v247
	v_max_f32_e32 v250, 0xda24260, v250
	v_max_f32_e32 v251, 0xda24260, v251
	v_rcp_f32_e32 v246, v246
	v_rcp_f32_e32 v247, v247
	v_rcp_f32_e32 v250, v250
	v_rcp_f32_e32 v251, v251
	v_lshlrev_b32_e32 v248, 16, v236
	v_and_b32_e32 v249, 0xffff0000, v236
	v_lshlrev_b32_e32 v252, 16, v237
	v_and_b32_e32 v253, 0xffff0000, v237
	v_pk_mul_f32 v[246:247], v[246:247], v[248:249]
	v_pk_mul_f32 v[250:251], v[250:251], v[252:253]
	v_pk_mul_f32 v[108:109], v[108:109], v[246:247]
	v_pk_mul_f32 v[110:111], v[110:111], v[250:251]
	global_load_dwordx4 v[234:237], v[176:177], off offset:256
	global_load_dwordx4 v[238:241], v[166:167], off offset:256
	v_lshl_add_u64 v[176:177], v[176:177], 0, v[180:181]
	v_lshl_add_u64 v[166:167], v[166:167], 0, v[180:181]
	s_waitcnt vmcnt(8)
	v_lshlrev_b32_e32 v246, 16, v136
	v_and_b32_e32 v247, 0xffff0000, v136
	v_lshlrev_b32_e32 v250, 16, v137
	v_and_b32_e32 v251, 0xffff0000, v137
	v_max_f32_e32 v246, 0xda24260, v246
	v_max_f32_e32 v247, 0xda24260, v247
	v_max_f32_e32 v250, 0xda24260, v250
	v_max_f32_e32 v251, 0xda24260, v251
	v_rcp_f32_e32 v246, v246
	v_rcp_f32_e32 v247, v247
	v_rcp_f32_e32 v250, v250
	v_rcp_f32_e32 v251, v251
	v_lshlrev_b32_e32 v248, 16, v132
	v_and_b32_e32 v249, 0xffff0000, v132
	v_lshlrev_b32_e32 v252, 16, v133
	v_and_b32_e32 v253, 0xffff0000, v133
	v_pk_mul_f32 v[246:247], v[246:247], v[248:249]
	v_pk_mul_f32 v[250:251], v[250:251], v[252:253]
	v_pk_mul_f32 v[80:81], v[80:81], v[246:247]
	v_pk_mul_f32 v[82:83], v[82:83], v[250:251]
	v_lshlrev_b32_e32 v246, 16, v138
	v_and_b32_e32 v247, 0xffff0000, v138
	v_lshlrev_b32_e32 v250, 16, v139
	v_and_b32_e32 v251, 0xffff0000, v139
	v_max_f32_e32 v246, 0xda24260, v246
	v_max_f32_e32 v247, 0xda24260, v247
	v_max_f32_e32 v250, 0xda24260, v250
	v_max_f32_e32 v251, 0xda24260, v251
	v_rcp_f32_e32 v246, v246
	v_rcp_f32_e32 v247, v247
	v_rcp_f32_e32 v250, v250
	v_rcp_f32_e32 v251, v251
	v_lshlrev_b32_e32 v248, 16, v134
	v_and_b32_e32 v249, 0xffff0000, v134
	v_lshlrev_b32_e32 v252, 16, v135
	v_and_b32_e32 v253, 0xffff0000, v135
	v_pk_mul_f32 v[246:247], v[246:247], v[248:249]
	v_pk_mul_f32 v[250:251], v[250:251], v[252:253]
	v_pk_mul_f32 v[76:77], v[76:77], v[246:247]
	v_pk_mul_f32 v[78:79], v[78:79], v[250:251]
	global_load_dwordx4 v[132:135], v[176:177], off
	global_load_dwordx4 v[136:139], v[166:167], off
	s_waitcnt vmcnt(8)
	v_lshlrev_b32_e32 v246, 16, v154
	v_and_b32_e32 v247, 0xffff0000, v154
	v_lshlrev_b32_e32 v250, 16, v155
	v_and_b32_e32 v251, 0xffff0000, v155
	v_max_f32_e32 v246, 0xda24260, v246
	v_max_f32_e32 v247, 0xda24260, v247
	v_max_f32_e32 v250, 0xda24260, v250
	v_max_f32_e32 v251, 0xda24260, v251
	v_rcp_f32_e32 v246, v246
	v_rcp_f32_e32 v247, v247
	v_rcp_f32_e32 v250, v250
	v_rcp_f32_e32 v251, v251
	v_lshlrev_b32_e32 v248, 16, v150
	v_and_b32_e32 v249, 0xffff0000, v150
	v_lshlrev_b32_e32 v252, 16, v151
	v_and_b32_e32 v253, 0xffff0000, v151
	v_pk_mul_f32 v[246:247], v[246:247], v[248:249]
	v_pk_mul_f32 v[250:251], v[250:251], v[252:253]
	v_pk_mul_f32 v[104:105], v[104:105], v[246:247]
	v_pk_mul_f32 v[106:107], v[106:107], v[250:251]
	v_lshlrev_b32_e32 v246, 16, v156
	v_and_b32_e32 v247, 0xffff0000, v156
	v_lshlrev_b32_e32 v250, 16, v157
	v_and_b32_e32 v251, 0xffff0000, v157
	v_max_f32_e32 v246, 0xda24260, v246
	v_max_f32_e32 v247, 0xda24260, v247
	v_max_f32_e32 v250, 0xda24260, v250
	v_max_f32_e32 v251, 0xda24260, v251
	v_rcp_f32_e32 v246, v246
	v_rcp_f32_e32 v247, v247
	v_rcp_f32_e32 v250, v250
	v_rcp_f32_e32 v251, v251
	v_lshlrev_b32_e32 v248, 16, v152
	v_and_b32_e32 v249, 0xffff0000, v152
	v_lshlrev_b32_e32 v252, 16, v153
	v_and_b32_e32 v253, 0xffff0000, v153
	v_pk_mul_f32 v[246:247], v[246:247], v[248:249]
	v_pk_mul_f32 v[250:251], v[250:251], v[252:253]
	v_pk_mul_f32 v[100:101], v[100:101], v[246:247]
	v_pk_mul_f32 v[102:103], v[102:103], v[250:251]
	global_load_dwordx4 v[150:153], v[176:177], off offset:256
	global_load_dwordx4 v[154:157], v[166:167], off offset:256
	v_lshl_add_u64 v[176:177], v[176:177], 0, v[180:181]
	v_lshl_add_u64 v[166:167], v[166:167], 0, v[180:181]
	s_waitcnt vmcnt(8)
	v_lshlrev_b32_e32 v246, 16, v162
	v_and_b32_e32 v247, 0xffff0000, v162
	v_lshlrev_b32_e32 v250, 16, v163
	v_and_b32_e32 v251, 0xffff0000, v163
	v_max_f32_e32 v246, 0xda24260, v246
	v_max_f32_e32 v247, 0xda24260, v247
	v_max_f32_e32 v250, 0xda24260, v250
	v_max_f32_e32 v251, 0xda24260, v251
	v_rcp_f32_e32 v246, v246
	v_rcp_f32_e32 v247, v247
	v_rcp_f32_e32 v250, v250
	v_rcp_f32_e32 v251, v251
	v_lshlrev_b32_e32 v248, 16, v158
	v_and_b32_e32 v249, 0xffff0000, v158
	v_lshlrev_b32_e32 v252, 16, v159
	v_and_b32_e32 v253, 0xffff0000, v159
	v_pk_mul_f32 v[246:247], v[246:247], v[248:249]
	v_pk_mul_f32 v[250:251], v[250:251], v[252:253]
	v_pk_mul_f32 v[72:73], v[72:73], v[246:247]
	v_pk_mul_f32 v[74:75], v[74:75], v[250:251]
	v_lshlrev_b32_e32 v246, 16, v164
	v_and_b32_e32 v247, 0xffff0000, v164
	v_lshlrev_b32_e32 v250, 16, v165
	v_and_b32_e32 v251, 0xffff0000, v165
	v_max_f32_e32 v246, 0xda24260, v246
	v_max_f32_e32 v247, 0xda24260, v247
	v_max_f32_e32 v250, 0xda24260, v250
	v_max_f32_e32 v251, 0xda24260, v251
	v_rcp_f32_e32 v246, v246
	v_rcp_f32_e32 v247, v247
	v_rcp_f32_e32 v250, v250
	v_rcp_f32_e32 v251, v251
	v_lshlrev_b32_e32 v248, 16, v160
	v_and_b32_e32 v249, 0xffff0000, v160
	v_lshlrev_b32_e32 v252, 16, v161
	v_and_b32_e32 v253, 0xffff0000, v161
	v_pk_mul_f32 v[246:247], v[246:247], v[248:249]
	v_pk_mul_f32 v[250:251], v[250:251], v[252:253]
	v_pk_mul_f32 v[68:69], v[68:69], v[246:247]
	v_pk_mul_f32 v[70:71], v[70:71], v[250:251]
	global_load_dwordx4 v[158:161], v[176:177], off
	global_load_dwordx4 v[162:165], v[166:167], off
	s_waitcnt vmcnt(8)
	v_lshlrev_b32_e32 v246, 16, v230
	v_and_b32_e32 v247, 0xffff0000, v230
	v_lshlrev_b32_e32 v250, 16, v231
	v_and_b32_e32 v251, 0xffff0000, v231
	v_max_f32_e32 v246, 0xda24260, v246
	v_max_f32_e32 v247, 0xda24260, v247
	v_max_f32_e32 v250, 0xda24260, v250
	v_max_f32_e32 v251, 0xda24260, v251
	v_rcp_f32_e32 v246, v246
	v_rcp_f32_e32 v247, v247
	v_rcp_f32_e32 v250, v250
	v_rcp_f32_e32 v251, v251
	v_lshlrev_b32_e32 v248, 16, v172
	v_and_b32_e32 v249, 0xffff0000, v172
	v_lshlrev_b32_e32 v252, 16, v173
	v_and_b32_e32 v253, 0xffff0000, v173
	v_pk_mul_f32 v[246:247], v[246:247], v[248:249]
	v_pk_mul_f32 v[250:251], v[250:251], v[252:253]
	v_pk_mul_f32 v[64:65], v[64:65], v[246:247]
	v_pk_mul_f32 v[66:67], v[66:67], v[250:251]
	v_lshlrev_b32_e32 v246, 16, v232
	v_and_b32_e32 v247, 0xffff0000, v232
	v_lshlrev_b32_e32 v250, 16, v233
	v_and_b32_e32 v251, 0xffff0000, v233
	v_max_f32_e32 v246, 0xda24260, v246
	v_max_f32_e32 v247, 0xda24260, v247
	v_max_f32_e32 v250, 0xda24260, v250
	v_max_f32_e32 v251, 0xda24260, v251
	v_rcp_f32_e32 v246, v246
	v_rcp_f32_e32 v247, v247
	v_rcp_f32_e32 v250, v250
	v_rcp_f32_e32 v251, v251
	v_lshlrev_b32_e32 v248, 16, v174
	v_and_b32_e32 v249, 0xffff0000, v174
	v_lshlrev_b32_e32 v252, 16, v175
	v_and_b32_e32 v253, 0xffff0000, v175
	v_pk_mul_f32 v[246:247], v[246:247], v[248:249]
	v_pk_mul_f32 v[250:251], v[250:251], v[252:253]
	v_pk_mul_f32 v[60:61], v[60:61], v[246:247]
	v_pk_mul_f32 v[62:63], v[62:63], v[250:251]
	global_load_dwordx4 v[172:175], v[176:177], off offset:256
	global_load_dwordx4 v[230:233], v[166:167], off offset:256
	v_lshl_add_u64 v[176:177], v[176:177], 0, v[180:181]
	v_lshl_add_u64 v[166:167], v[166:167], 0, v[180:181]
	s_waitcnt vmcnt(8)
	v_lshlrev_b32_e32 v246, 16, v238
	v_and_b32_e32 v247, 0xffff0000, v238
	v_lshlrev_b32_e32 v250, 16, v239
	v_and_b32_e32 v251, 0xffff0000, v239
	v_max_f32_e32 v246, 0xda24260, v246
	v_max_f32_e32 v247, 0xda24260, v247
	v_max_f32_e32 v250, 0xda24260, v250
	v_max_f32_e32 v251, 0xda24260, v251
	v_rcp_f32_e32 v246, v246
	v_rcp_f32_e32 v247, v247
	v_rcp_f32_e32 v250, v250
	v_rcp_f32_e32 v251, v251
	v_lshlrev_b32_e32 v248, 16, v234
	v_and_b32_e32 v249, 0xffff0000, v234
	v_lshlrev_b32_e32 v252, 16, v235
	v_and_b32_e32 v253, 0xffff0000, v235
	v_pk_mul_f32 v[246:247], v[246:247], v[248:249]
	v_pk_mul_f32 v[250:251], v[250:251], v[252:253]
	v_pk_mul_f32 v[32:33], v[32:33], v[246:247]
	v_pk_mul_f32 v[34:35], v[34:35], v[250:251]
	v_lshlrev_b32_e32 v246, 16, v240
	v_and_b32_e32 v247, 0xffff0000, v240
	v_lshlrev_b32_e32 v250, 16, v241
	v_and_b32_e32 v251, 0xffff0000, v241
	v_max_f32_e32 v246, 0xda24260, v246
	v_max_f32_e32 v247, 0xda24260, v247
	v_max_f32_e32 v250, 0xda24260, v250
	v_max_f32_e32 v251, 0xda24260, v251
	v_rcp_f32_e32 v246, v246
	v_rcp_f32_e32 v247, v247
	v_rcp_f32_e32 v250, v250
	v_rcp_f32_e32 v251, v251
	v_lshlrev_b32_e32 v248, 16, v236
	v_and_b32_e32 v249, 0xffff0000, v236
	v_lshlrev_b32_e32 v252, 16, v237
	v_and_b32_e32 v253, 0xffff0000, v237
	v_pk_mul_f32 v[246:247], v[246:247], v[248:249]
	v_pk_mul_f32 v[250:251], v[250:251], v[252:253]
	v_pk_mul_f32 v[28:29], v[28:29], v[246:247]
	v_pk_mul_f32 v[30:31], v[30:31], v[250:251]
	global_load_dwordx4 v[234:237], v[176:177], off
	global_load_dwordx4 v[238:241], v[166:167], off
	s_waitcnt vmcnt(8)
	v_lshlrev_b32_e32 v246, 16, v136
	v_and_b32_e32 v247, 0xffff0000, v136
	v_lshlrev_b32_e32 v250, 16, v137
	v_and_b32_e32 v251, 0xffff0000, v137
	v_max_f32_e32 v246, 0xda24260, v246
	v_max_f32_e32 v247, 0xda24260, v247
	v_max_f32_e32 v250, 0xda24260, v250
	v_max_f32_e32 v251, 0xda24260, v251
	v_rcp_f32_e32 v246, v246
	v_rcp_f32_e32 v247, v247
	v_rcp_f32_e32 v250, v250
	v_rcp_f32_e32 v251, v251
	v_lshlrev_b32_e32 v248, 16, v132
	v_and_b32_e32 v249, 0xffff0000, v132
	v_lshlrev_b32_e32 v252, 16, v133
	v_and_b32_e32 v253, 0xffff0000, v133
	v_pk_mul_f32 v[246:247], v[246:247], v[248:249]
	v_pk_mul_f32 v[250:251], v[250:251], v[252:253]
	v_pk_mul_f32 v[56:57], v[56:57], v[246:247]
	v_pk_mul_f32 v[58:59], v[58:59], v[250:251]
	v_lshlrev_b32_e32 v246, 16, v138
	v_and_b32_e32 v247, 0xffff0000, v138
	v_lshlrev_b32_e32 v250, 16, v139
	v_and_b32_e32 v251, 0xffff0000, v139
	v_max_f32_e32 v246, 0xda24260, v246
	v_max_f32_e32 v247, 0xda24260, v247
	v_max_f32_e32 v250, 0xda24260, v250
	v_max_f32_e32 v251, 0xda24260, v251
	v_rcp_f32_e32 v246, v246
	v_rcp_f32_e32 v247, v247
	v_rcp_f32_e32 v250, v250
	v_rcp_f32_e32 v251, v251
	v_lshlrev_b32_e32 v248, 16, v134
	v_and_b32_e32 v249, 0xffff0000, v134
	v_lshlrev_b32_e32 v252, 16, v135
	v_and_b32_e32 v253, 0xffff0000, v135
	v_pk_mul_f32 v[246:247], v[246:247], v[248:249]
	v_pk_mul_f32 v[250:251], v[250:251], v[252:253]
	v_pk_mul_f32 v[52:53], v[52:53], v[246:247]
	v_pk_mul_f32 v[54:55], v[54:55], v[250:251]
	global_load_dwordx4 v[132:135], v[176:177], off offset:256
	global_load_dwordx4 v[136:139], v[166:167], off offset:256
	s_waitcnt vmcnt(8)
	v_lshlrev_b32_e32 v246, 16, v154
	v_and_b32_e32 v247, 0xffff0000, v154
	v_lshlrev_b32_e32 v250, 16, v155
	v_and_b32_e32 v251, 0xffff0000, v155
	v_max_f32_e32 v246, 0xda24260, v246
	v_max_f32_e32 v247, 0xda24260, v247
	v_max_f32_e32 v250, 0xda24260, v250
	v_max_f32_e32 v251, 0xda24260, v251
	v_rcp_f32_e32 v246, v246
	v_rcp_f32_e32 v247, v247
	v_rcp_f32_e32 v250, v250
	v_rcp_f32_e32 v251, v251
	v_lshlrev_b32_e32 v248, 16, v150
	v_and_b32_e32 v249, 0xffff0000, v150
	v_lshlrev_b32_e32 v252, 16, v151
	v_and_b32_e32 v253, 0xffff0000, v151
	v_pk_mul_f32 v[246:247], v[246:247], v[248:249]
	v_pk_mul_f32 v[250:251], v[250:251], v[252:253]
	v_pk_mul_f32 v[24:25], v[24:25], v[246:247]
	v_pk_mul_f32 v[26:27], v[26:27], v[250:251]
	v_lshlrev_b32_e32 v246, 16, v156
	v_and_b32_e32 v247, 0xffff0000, v156
	v_lshlrev_b32_e32 v250, 16, v157
	v_and_b32_e32 v251, 0xffff0000, v157
	v_max_f32_e32 v246, 0xda24260, v246
	v_max_f32_e32 v247, 0xda24260, v247
	v_max_f32_e32 v250, 0xda24260, v250
	v_max_f32_e32 v251, 0xda24260, v251
	v_rcp_f32_e32 v246, v246
	v_rcp_f32_e32 v247, v247
	v_rcp_f32_e32 v250, v250
	v_rcp_f32_e32 v251, v251
	v_lshlrev_b32_e32 v248, 16, v152
	v_and_b32_e32 v249, 0xffff0000, v152
	v_lshlrev_b32_e32 v252, 16, v153
	v_and_b32_e32 v253, 0xffff0000, v153
	v_pk_mul_f32 v[246:247], v[246:247], v[248:249]
	v_pk_mul_f32 v[250:251], v[250:251], v[252:253]
	v_pk_mul_f32 v[20:21], v[20:21], v[246:247]
	v_pk_mul_f32 v[22:23], v[22:23], v[250:251]
	s_waitcnt vmcnt(6)
	v_lshlrev_b32_e32 v246, 16, v162
	v_and_b32_e32 v247, 0xffff0000, v162
	v_lshlrev_b32_e32 v250, 16, v163
	v_and_b32_e32 v251, 0xffff0000, v163
	v_max_f32_e32 v246, 0xda24260, v246
	v_max_f32_e32 v247, 0xda24260, v247
	v_max_f32_e32 v250, 0xda24260, v250
	v_max_f32_e32 v251, 0xda24260, v251
	v_rcp_f32_e32 v246, v246
	v_rcp_f32_e32 v247, v247
	v_rcp_f32_e32 v250, v250
	v_rcp_f32_e32 v251, v251
	v_lshlrev_b32_e32 v248, 16, v158
	v_and_b32_e32 v249, 0xffff0000, v158
	v_lshlrev_b32_e32 v252, 16, v159
	v_and_b32_e32 v253, 0xffff0000, v159
	v_pk_mul_f32 v[246:247], v[246:247], v[248:249]
	v_pk_mul_f32 v[250:251], v[250:251], v[252:253]
	v_pk_mul_f32 v[48:49], v[48:49], v[246:247]
	v_pk_mul_f32 v[50:51], v[50:51], v[250:251]
	v_lshlrev_b32_e32 v246, 16, v164
	v_and_b32_e32 v247, 0xffff0000, v164
	v_lshlrev_b32_e32 v250, 16, v165
	v_and_b32_e32 v251, 0xffff0000, v165
	v_max_f32_e32 v246, 0xda24260, v246
	v_max_f32_e32 v247, 0xda24260, v247
	v_max_f32_e32 v250, 0xda24260, v250
	v_max_f32_e32 v251, 0xda24260, v251
	v_rcp_f32_e32 v246, v246
	v_rcp_f32_e32 v247, v247
	v_rcp_f32_e32 v250, v250
	v_rcp_f32_e32 v251, v251
	v_lshlrev_b32_e32 v248, 16, v160
	v_and_b32_e32 v249, 0xffff0000, v160
	v_lshlrev_b32_e32 v252, 16, v161
	v_and_b32_e32 v253, 0xffff0000, v161
	v_pk_mul_f32 v[246:247], v[246:247], v[248:249]
	v_pk_mul_f32 v[250:251], v[250:251], v[252:253]
	v_pk_mul_f32 v[44:45], v[44:45], v[246:247]
	v_pk_mul_f32 v[46:47], v[46:47], v[250:251]
	s_waitcnt vmcnt(4)
	v_lshlrev_b32_e32 v246, 16, v230
	v_and_b32_e32 v247, 0xffff0000, v230
	v_lshlrev_b32_e32 v250, 16, v231
	v_and_b32_e32 v251, 0xffff0000, v231
	v_max_f32_e32 v246, 0xda24260, v246
	v_max_f32_e32 v247, 0xda24260, v247
	v_max_f32_e32 v250, 0xda24260, v250
	v_max_f32_e32 v251, 0xda24260, v251
	v_rcp_f32_e32 v246, v246
	v_rcp_f32_e32 v247, v247
	v_rcp_f32_e32 v250, v250
	v_rcp_f32_e32 v251, v251
	v_lshlrev_b32_e32 v248, 16, v172
	v_and_b32_e32 v249, 0xffff0000, v172
	v_lshlrev_b32_e32 v252, 16, v173
	v_and_b32_e32 v253, 0xffff0000, v173
	v_pk_mul_f32 v[246:247], v[246:247], v[248:249]
	v_pk_mul_f32 v[250:251], v[250:251], v[252:253]
	v_pk_mul_f32 v[16:17], v[16:17], v[246:247]
	v_pk_mul_f32 v[18:19], v[18:19], v[250:251]
	v_lshlrev_b32_e32 v246, 16, v232
	v_and_b32_e32 v247, 0xffff0000, v232
	v_lshlrev_b32_e32 v250, 16, v233
	v_and_b32_e32 v251, 0xffff0000, v233
	v_max_f32_e32 v246, 0xda24260, v246
	v_max_f32_e32 v247, 0xda24260, v247
	v_max_f32_e32 v250, 0xda24260, v250
	v_max_f32_e32 v251, 0xda24260, v251
	v_rcp_f32_e32 v246, v246
	v_rcp_f32_e32 v247, v247
	v_rcp_f32_e32 v250, v250
	v_rcp_f32_e32 v251, v251
	v_lshlrev_b32_e32 v248, 16, v174
	v_and_b32_e32 v249, 0xffff0000, v174
	v_lshlrev_b32_e32 v252, 16, v175
	v_and_b32_e32 v253, 0xffff0000, v175
	v_pk_mul_f32 v[246:247], v[246:247], v[248:249]
	v_pk_mul_f32 v[250:251], v[250:251], v[252:253]
	v_pk_mul_f32 v[12:13], v[12:13], v[246:247]
	v_pk_mul_f32 v[14:15], v[14:15], v[250:251]
	s_waitcnt vmcnt(2)
	v_lshlrev_b32_e32 v246, 16, v238
	v_and_b32_e32 v247, 0xffff0000, v238
	v_lshlrev_b32_e32 v250, 16, v239
	v_and_b32_e32 v251, 0xffff0000, v239
	v_max_f32_e32 v246, 0xda24260, v246
	v_max_f32_e32 v247, 0xda24260, v247
	v_max_f32_e32 v250, 0xda24260, v250
	v_max_f32_e32 v251, 0xda24260, v251
	v_rcp_f32_e32 v246, v246
	v_rcp_f32_e32 v247, v247
	v_rcp_f32_e32 v250, v250
	v_rcp_f32_e32 v251, v251
	v_lshlrev_b32_e32 v248, 16, v234
	v_and_b32_e32 v249, 0xffff0000, v234
	v_lshlrev_b32_e32 v252, 16, v235
	v_and_b32_e32 v253, 0xffff0000, v235
	v_pk_mul_f32 v[246:247], v[246:247], v[248:249]
	v_pk_mul_f32 v[250:251], v[250:251], v[252:253]
	v_pk_mul_f32 v[40:41], v[40:41], v[246:247]
	v_pk_mul_f32 v[42:43], v[42:43], v[250:251]
	v_lshlrev_b32_e32 v246, 16, v240
	v_and_b32_e32 v247, 0xffff0000, v240
	v_lshlrev_b32_e32 v250, 16, v241
	v_and_b32_e32 v251, 0xffff0000, v241
	v_max_f32_e32 v246, 0xda24260, v246
	v_max_f32_e32 v247, 0xda24260, v247
	v_max_f32_e32 v250, 0xda24260, v250
	v_max_f32_e32 v251, 0xda24260, v251
	v_rcp_f32_e32 v246, v246
	v_rcp_f32_e32 v247, v247
	v_rcp_f32_e32 v250, v250
	v_rcp_f32_e32 v251, v251
	v_lshlrev_b32_e32 v248, 16, v236
	v_and_b32_e32 v249, 0xffff0000, v236
	v_lshlrev_b32_e32 v252, 16, v237
	v_and_b32_e32 v253, 0xffff0000, v237
	v_pk_mul_f32 v[246:247], v[246:247], v[248:249]
	v_pk_mul_f32 v[250:251], v[250:251], v[252:253]
	v_pk_mul_f32 v[36:37], v[36:37], v[246:247]
	v_pk_mul_f32 v[38:39], v[38:39], v[250:251]
	s_waitcnt vmcnt(0)
	v_lshlrev_b32_e32 v246, 16, v136
	v_and_b32_e32 v247, 0xffff0000, v136
	v_lshlrev_b32_e32 v250, 16, v137
	v_and_b32_e32 v251, 0xffff0000, v137
	v_max_f32_e32 v246, 0xda24260, v246
	v_max_f32_e32 v247, 0xda24260, v247
	v_max_f32_e32 v250, 0xda24260, v250
	v_max_f32_e32 v251, 0xda24260, v251
	v_rcp_f32_e32 v246, v246
	v_rcp_f32_e32 v247, v247
	v_rcp_f32_e32 v250, v250
	v_rcp_f32_e32 v251, v251
	v_lshlrev_b32_e32 v248, 16, v132
	v_and_b32_e32 v249, 0xffff0000, v132
	v_lshlrev_b32_e32 v252, 16, v133
	v_and_b32_e32 v253, 0xffff0000, v133
	v_pk_mul_f32 v[246:247], v[246:247], v[248:249]
	v_pk_mul_f32 v[250:251], v[250:251], v[252:253]
	v_pk_mul_f32 v[8:9], v[8:9], v[246:247]
	v_pk_mul_f32 v[10:11], v[10:11], v[250:251]
	v_lshlrev_b32_e32 v246, 16, v138
	v_and_b32_e32 v247, 0xffff0000, v138
	v_lshlrev_b32_e32 v250, 16, v139
	v_and_b32_e32 v251, 0xffff0000, v139
	v_max_f32_e32 v246, 0xda24260, v246
	v_max_f32_e32 v247, 0xda24260, v247
	v_max_f32_e32 v250, 0xda24260, v250
	v_max_f32_e32 v251, 0xda24260, v251
	v_rcp_f32_e32 v246, v246
	v_rcp_f32_e32 v247, v247
	v_rcp_f32_e32 v250, v250
	v_rcp_f32_e32 v251, v251
	v_lshlrev_b32_e32 v248, 16, v134
	v_and_b32_e32 v249, 0xffff0000, v134
	v_lshlrev_b32_e32 v252, 16, v135
	v_and_b32_e32 v253, 0xffff0000, v135
	v_pk_mul_f32 v[246:247], v[246:247], v[248:249]
	v_pk_mul_f32 v[250:251], v[250:251], v[252:253]
	v_pk_mul_f32 v[4:5], v[4:5], v[246:247]
	v_pk_mul_f32 v[6:7], v[6:7], v[250:251]
